# P2 + P8 + P12 residual ladders pipelined with bf16 stores after the row-statistics publish; P7 gain loads hoisted
# baseline (speedup 1.0000x reference)
.LBB0_335:
	s_lshl_b32 s93, s10, 8
	v_lshrrev_b32_e32 v2, 2, v186
	s_lshl_b32 s94, s16, 5
	v_and_b32_e32 v168, 12, v2
	v_add_u32_e32 v26, s93, v184
	v_or_b32_e32 v170, s94, v168
	v_ashrrev_i32_e32 v27, 31, v26
	v_or_b32_e32 v162, s60, v170
	v_lshlrev_b64 v[166:167], 12, v[26:27]
	v_readlane_b32 s40, v247, 6
	v_or_b32_e32 v166, v166, v162
	v_readlane_b32 s41, v247, 7
	s_barrier
	v_lshlrev_b32_e32 v244, 2, v166
	v_lshlrev_b32_e32 v187, 1, v166
	s_nop 4
	global_load_dwordx4 v[188:191], v244, s[40:41]
	global_load_dwordx4 v[192:195], v244, s[40:41] offset:64
	global_load_dwordx4 v[196:199], v244, s[40:41] offset:512
	global_load_dwordx4 v[200:203], v244, s[40:41] offset:576
	v_add_u32_e32 v245, 0x40000, v244
	global_load_dwordx4 v[204:207], v245, s[40:41]
	global_load_dwordx4 v[208:211], v245, s[40:41] offset:64
	global_load_dwordx4 v[212:215], v245, s[40:41] offset:512
	global_load_dwordx4 v[216:219], v245, s[40:41] offset:576
	v_add_u32_e32 v245, 0x80000, v244
	global_load_dwordx4 v[220:223], v245, s[40:41]
	global_load_dwordx4 v[224:227], v245, s[40:41] offset:64
	global_load_dwordx4 v[228:231], v245, s[40:41] offset:512
	global_load_dwordx4 v[232:235], v245, s[40:41] offset:576
	v_add_u32_e32 v245, 0xc0000, v244
	global_load_dwordx4 v[236:239], v245, s[40:41]
	global_load_dwordx4 v[240:243], v245, s[40:41] offset:64
	v_and_b32_e32 v171, 63, v186
	v_readlane_b32 s42, v247, 8
	v_readlane_b32 s43, v247, 9
	v_readlane_b32 s44, v247, 10
	v_readlane_b32 s45, v247, 11
	v_readlane_b32 s46, v247, 12
	v_readlane_b32 s47, v247, 13
	v_readlane_b32 s48, v247, 14
	v_readlane_b32 s49, v247, 15
	v_readlane_b32 s50, v247, 16
	v_readlane_b32 s51, v247, 17
	v_readlane_b32 s52, v247, 18
	v_readlane_b32 s53, v247, 19
	v_readlane_b32 s54, v247, 20
	v_readlane_b32 s55, v247, 21
	s_waitcnt vmcnt(12)
	v_pk_fma_f32 v[72:73], v[72:73], s[58:59], v[190:191] op_sel_hi:[1,0,1]
	v_pk_fma_f32 v[70:71], v[70:71], s[58:59], v[188:189] op_sel_hi:[1,0,1]
	v_pk_fma_f32 v[68:69], v[68:69], s[58:59], v[194:195] op_sel_hi:[1,0,1]
	v_pk_fma_f32 v[66:67], v[66:67], s[58:59], v[192:193] op_sel_hi:[1,0,1]
	v_add_u32_e32 v245, 0xc0000, v244
	global_load_dwordx4 v[188:191], v245, s[40:41] offset:512
	global_load_dwordx4 v[192:195], v245, s[40:41] offset:576
	s_waitcnt vmcnt(12)
	v_pk_fma_f32 v[8:9], v[160:161], s[58:59], v[198:199] op_sel_hi:[1,0,1]
	v_pk_fma_f32 v[6:7], v[158:159], s[58:59], v[196:197] op_sel_hi:[1,0,1]
	v_pk_fma_f32 v[2:3], v[154:155], s[58:59], v[200:201] op_sel_hi:[1,0,1]
	v_pk_fma_f32 v[4:5], v[156:157], s[58:59], v[202:203] op_sel_hi:[1,0,1]
	v_add_u32_e32 v245, 0x200000, v244
	global_load_dwordx4 v[196:199], v245, s[40:41]
	global_load_dwordx4 v[200:203], v245, s[40:41] offset:64
	s_waitcnt vmcnt(12)
	v_pk_fma_f32 v[80:81], v[80:81], s[58:59], v[206:207] op_sel_hi:[1,0,1]
	v_pk_fma_f32 v[78:79], v[78:79], s[58:59], v[204:205] op_sel_hi:[1,0,1]
	v_pk_fma_f32 v[76:77], v[76:77], s[58:59], v[210:211] op_sel_hi:[1,0,1]
	v_pk_fma_f32 v[74:75], v[74:75], s[58:59], v[208:209] op_sel_hi:[1,0,1]
	v_add_u32_e32 v245, 0x200000, v244
	global_load_dwordx4 v[204:207], v245, s[40:41] offset:512
	global_load_dwordx4 v[208:211], v245, s[40:41] offset:576
	s_waitcnt vmcnt(12)
	v_pk_fma_f32 v[16:17], v[152:153], s[58:59], v[214:215] op_sel_hi:[1,0,1]
	v_pk_fma_f32 v[14:15], v[150:151], s[58:59], v[212:213] op_sel_hi:[1,0,1]
	v_pk_fma_f32 v[10:11], v[146:147], s[58:59], v[216:217] op_sel_hi:[1,0,1]
	v_pk_fma_f32 v[12:13], v[148:149], s[58:59], v[218:219] op_sel_hi:[1,0,1]
	v_add_u32_e32 v245, 0x240000, v244
	global_load_dwordx4 v[212:215], v245, s[40:41]
	global_load_dwordx4 v[216:219], v245, s[40:41] offset:64
	s_waitcnt vmcnt(12)
	v_pk_fma_f32 v[88:89], v[88:89], s[58:59], v[222:223] op_sel_hi:[1,0,1]
	v_pk_fma_f32 v[86:87], v[86:87], s[58:59], v[220:221] op_sel_hi:[1,0,1]
	v_pk_fma_f32 v[84:85], v[84:85], s[58:59], v[226:227] op_sel_hi:[1,0,1]
	v_pk_fma_f32 v[82:83], v[82:83], s[58:59], v[224:225] op_sel_hi:[1,0,1]
	v_add_u32_e32 v245, 0x240000, v244
	global_load_dwordx4 v[220:223], v245, s[40:41] offset:512
	global_load_dwordx4 v[224:227], v245, s[40:41] offset:576
	s_waitcnt vmcnt(12)
	v_pk_fma_f32 v[22:23], v[142:143], s[58:59], v[228:229] op_sel_hi:[1,0,1]
	v_pk_fma_f32 v[18:19], v[138:139], s[58:59], v[232:233] op_sel_hi:[1,0,1]
	v_pk_fma_f32 v[24:25], v[144:145], s[58:59], v[230:231] op_sel_hi:[1,0,1]
	v_pk_fma_f32 v[20:21], v[140:141], s[58:59], v[234:235] op_sel_hi:[1,0,1]
	v_add_u32_e32 v245, 0x280000, v244
	global_load_dwordx4 v[228:231], v245, s[40:41]
	global_load_dwordx4 v[232:235], v245, s[40:41] offset:64
	s_waitcnt vmcnt(12)
	v_pk_fma_f32 v[96:97], v[96:97], s[58:59], v[238:239] op_sel_hi:[1,0,1]
	v_pk_fma_f32 v[94:95], v[94:95], s[58:59], v[236:237] op_sel_hi:[1,0,1]
	v_pk_fma_f32 v[92:93], v[92:93], s[58:59], v[242:243] op_sel_hi:[1,0,1]
	v_pk_fma_f32 v[90:91], v[90:91], s[58:59], v[240:241] op_sel_hi:[1,0,1]
	v_add_u32_e32 v245, 0x280000, v244
	global_load_dwordx4 v[236:239], v245, s[40:41] offset:512
	global_load_dwordx4 v[240:243], v245, s[40:41] offset:576
	s_waitcnt vmcnt(12)
	v_pk_fma_f32 v[32:33], v[136:137], s[58:59], v[190:191] op_sel_hi:[1,0,1]
	v_pk_fma_f32 v[30:31], v[134:135], s[58:59], v[188:189] op_sel_hi:[1,0,1]
	v_pk_fma_f32 v[28:29], v[132:133], s[58:59], v[194:195] op_sel_hi:[1,0,1]
	v_pk_fma_f32 v[26:27], v[130:131], s[58:59], v[192:193] op_sel_hi:[1,0,1]
	v_add_u32_e32 v245, 0x2c0000, v244
	global_load_dwordx4 v[188:191], v245, s[40:41]
	global_load_dwordx4 v[192:195], v245, s[40:41] offset:64
	s_waitcnt vmcnt(12)
	v_pk_fma_f32 v[104:105], v[104:105], s[58:59], v[198:199] op_sel_hi:[1,0,1]
	v_pk_fma_f32 v[102:103], v[102:103], s[58:59], v[196:197] op_sel_hi:[1,0,1]
	v_pk_fma_f32 v[100:101], v[100:101], s[58:59], v[202:203] op_sel_hi:[1,0,1]
	v_pk_fma_f32 v[98:99], v[98:99], s[58:59], v[200:201] op_sel_hi:[1,0,1]
	v_add_u32_e32 v245, 0x2c0000, v244
	global_load_dwordx4 v[196:199], v245, s[40:41] offset:512
	global_load_dwordx4 v[200:203], v245, s[40:41] offset:576
	s_waitcnt vmcnt(12)
	v_pk_fma_f32 v[40:41], v[40:41], s[58:59], v[206:207] op_sel_hi:[1,0,1]
	v_pk_fma_f32 v[38:39], v[38:39], s[58:59], v[204:205] op_sel_hi:[1,0,1]
	v_pk_fma_f32 v[36:37], v[36:37], s[58:59], v[210:211] op_sel_hi:[1,0,1]
	v_pk_fma_f32 v[34:35], v[34:35], s[58:59], v[208:209] op_sel_hi:[1,0,1]
	s_waitcnt vmcnt(10)
	v_pk_fma_f32 v[112:113], v[112:113], s[58:59], v[214:215] op_sel_hi:[1,0,1]
	v_pk_fma_f32 v[110:111], v[110:111], s[58:59], v[212:213] op_sel_hi:[1,0,1]
	v_pk_fma_f32 v[108:109], v[108:109], s[58:59], v[218:219] op_sel_hi:[1,0,1]
	v_pk_fma_f32 v[106:107], v[106:107], s[58:59], v[216:217] op_sel_hi:[1,0,1]
	s_waitcnt vmcnt(8)
	v_pk_fma_f32 v[48:49], v[48:49], s[58:59], v[222:223] op_sel_hi:[1,0,1]
	v_pk_fma_f32 v[46:47], v[46:47], s[58:59], v[220:221] op_sel_hi:[1,0,1]
	v_pk_fma_f32 v[44:45], v[44:45], s[58:59], v[226:227] op_sel_hi:[1,0,1]
	v_pk_fma_f32 v[42:43], v[42:43], s[58:59], v[224:225] op_sel_hi:[1,0,1]
	s_waitcnt vmcnt(6)
	v_pk_fma_f32 v[120:121], v[120:121], s[58:59], v[230:231] op_sel_hi:[1,0,1]
	v_pk_fma_f32 v[118:119], v[118:119], s[58:59], v[228:229] op_sel_hi:[1,0,1]
	v_pk_fma_f32 v[116:117], v[116:117], s[58:59], v[234:235] op_sel_hi:[1,0,1]
	v_pk_fma_f32 v[114:115], v[114:115], s[58:59], v[232:233] op_sel_hi:[1,0,1]
	s_waitcnt vmcnt(4)
	v_pk_fma_f32 v[56:57], v[56:57], s[58:59], v[238:239] op_sel_hi:[1,0,1]
	v_pk_fma_f32 v[54:55], v[54:55], s[58:59], v[236:237] op_sel_hi:[1,0,1]
	v_pk_fma_f32 v[52:53], v[52:53], s[58:59], v[242:243] op_sel_hi:[1,0,1]
	v_pk_fma_f32 v[50:51], v[50:51], s[58:59], v[240:241] op_sel_hi:[1,0,1]
	s_waitcnt vmcnt(2)
	v_pk_fma_f32 v[128:129], v[128:129], s[58:59], v[190:191] op_sel_hi:[1,0,1]
	v_pk_fma_f32 v[126:127], v[126:127], s[58:59], v[188:189] op_sel_hi:[1,0,1]
	v_pk_fma_f32 v[124:125], v[124:125], s[58:59], v[194:195] op_sel_hi:[1,0,1]
	v_pk_fma_f32 v[122:123], v[122:123], s[58:59], v[192:193] op_sel_hi:[1,0,1]
	s_waitcnt vmcnt(0)
	v_pk_fma_f32 v[64:65], v[64:65], s[58:59], v[198:199] op_sel_hi:[1,0,1]
	v_pk_fma_f32 v[62:63], v[62:63], s[58:59], v[196:197] op_sel_hi:[1,0,1]
	v_pk_fma_f32 v[60:61], v[60:61], s[58:59], v[202:203] op_sel_hi:[1,0,1]
	v_pk_fma_f32 v[58:59], v[58:59], s[58:59], v[200:201] op_sel_hi:[1,0,1]
	s_lshl_b32 s0, s16, 2
	s_add_i32 s4, s0, 0
	v_mul_f32_e32 v134, v69, v69
	v_mul_f32_e32 v132, v71, v71
	v_mul_f32_e32 v133, v73, v73
	v_fmac_f32_e32 v132, v70, v70
	v_fmac_f32_e32 v133, v72, v72
	v_add_f32_e32 v132, v132, v133
	v_mul_f32_e32 v133, v67, v67
	v_fmac_f32_e32 v133, v66, v66
	v_fmac_f32_e32 v134, v68, v68
	v_add_f32_e32 v133, v133, v134
	v_add_f32_e32 v132, v132, v133
	v_mul_f32_e32 v133, v7, v7
	v_mul_f32_e32 v134, v9, v9
	v_fmac_f32_e32 v133, v6, v6
	v_fmac_f32_e32 v134, v8, v8
	v_and_b32_e32 v131, 64, v1
	v_add_f32_e32 v133, v133, v134
	v_xor_b32_e32 v130, 16, v1
	v_add_u32_e32 v155, 64, v131
	v_add_f32_e32 v132, v132, v133
	v_mul_f32_e32 v133, v3, v3
	v_mul_f32_e32 v134, v5, v5
	v_cmp_lt_i32_e32 vcc, v130, v155
	v_fmac_f32_e32 v133, v2, v2
	v_fmac_f32_e32 v134, v4, v4
	v_cndmask_b32_e32 v130, v1, v130, vcc
	v_add_f32_e32 v133, v133, v134
	v_lshlrev_b32_e32 v130, 2, v130
	v_add_f32_e32 v132, v133, v132
	ds_bpermute_b32 v133, v130, v132
	v_xor_b32_e32 v131, 32, v1
	v_cmp_lt_i32_e32 vcc, v131, v155
	s_waitcnt lgkmcnt(0)
	v_add_f32_e32 v132, v132, v133
	v_cndmask_b32_e32 v131, v1, v131, vcc
	v_lshlrev_b32_e32 v131, 2, v131
	ds_bpermute_b32 v133, v131, v132
	v_cmp_gt_u32_e32 vcc, 16, v171
	s_and_saveexec_b64 s[0:1], vcc
	s_cbranch_execz .LBB0_337
	s_lshl_b32 s5, s15, 10
	s_add_i32 s5, s4, s5
	v_lshl_add_u32 v134, v185, 4, s5
	s_waitcnt lgkmcnt(0)
	v_add_f32_e32 v132, v132, v133
	ds_write_b32 v134, v132

.LBB0_356:
	s_or_b64 exec, exec, s[12:13]
	v_cvt_pk_bf16_f32 v188, v70, v71
	v_cvt_pk_bf16_f32 v189, v72, v73
	v_cvt_pk_bf16_f32 v190, v66, v67
	v_cvt_pk_bf16_f32 v191, v68, v69
	global_store_dwordx2 v187, v[188:189], s[56:57]
	global_store_dwordx2 v187, v[190:191], s[56:57] offset:32
	v_cvt_pk_bf16_f32 v192, v6, v7
	v_cvt_pk_bf16_f32 v193, v8, v9
	v_cvt_pk_bf16_f32 v194, v2, v3
	v_cvt_pk_bf16_f32 v195, v4, v5
	global_store_dwordx2 v187, v[192:193], s[56:57] offset:256
	global_store_dwordx2 v187, v[194:195], s[56:57] offset:288
	v_add_u32_e32 v245, 0x20000, v187
	v_cvt_pk_bf16_f32 v188, v78, v79
	v_cvt_pk_bf16_f32 v189, v80, v81
	v_cvt_pk_bf16_f32 v190, v74, v75
	v_cvt_pk_bf16_f32 v191, v76, v77
	global_store_dwordx2 v245, v[188:189], s[56:57]
	global_store_dwordx2 v245, v[190:191], s[56:57] offset:32
	v_cvt_pk_bf16_f32 v192, v14, v15
	v_cvt_pk_bf16_f32 v193, v16, v17
	v_cvt_pk_bf16_f32 v194, v10, v11
	v_cvt_pk_bf16_f32 v195, v12, v13
	global_store_dwordx2 v245, v[192:193], s[56:57] offset:256
	global_store_dwordx2 v245, v[194:195], s[56:57] offset:288
	v_add_u32_e32 v245, 0x40000, v187
	v_cvt_pk_bf16_f32 v188, v86, v87
	v_cvt_pk_bf16_f32 v189, v88, v89
	v_cvt_pk_bf16_f32 v190, v82, v83
	v_cvt_pk_bf16_f32 v191, v84, v85
	global_store_dwordx2 v245, v[188:189], s[56:57]
	global_store_dwordx2 v245, v[190:191], s[56:57] offset:32
	v_cvt_pk_bf16_f32 v192, v22, v23
	v_cvt_pk_bf16_f32 v193, v24, v25
	v_cvt_pk_bf16_f32 v194, v18, v19
	v_cvt_pk_bf16_f32 v195, v20, v21
	global_store_dwordx2 v245, v[192:193], s[56:57] offset:256
	global_store_dwordx2 v245, v[194:195], s[56:57] offset:288
	v_add_u32_e32 v245, 0x60000, v187
	v_cvt_pk_bf16_f32 v188, v94, v95
	v_cvt_pk_bf16_f32 v189, v96, v97
	v_cvt_pk_bf16_f32 v190, v90, v91
	v_cvt_pk_bf16_f32 v191, v92, v93
	global_store_dwordx2 v245, v[188:189], s[56:57]
	global_store_dwordx2 v245, v[190:191], s[56:57] offset:32
	v_cvt_pk_bf16_f32 v192, v30, v31
	v_cvt_pk_bf16_f32 v193, v32, v33
	v_cvt_pk_bf16_f32 v194, v26, v27
	v_cvt_pk_bf16_f32 v195, v28, v29
	global_store_dwordx2 v245, v[192:193], s[56:57] offset:256
	global_store_dwordx2 v245, v[194:195], s[56:57] offset:288
	v_add_u32_e32 v245, 0x100000, v187
	v_cvt_pk_bf16_f32 v188, v102, v103
	v_cvt_pk_bf16_f32 v189, v104, v105
	v_cvt_pk_bf16_f32 v190, v98, v99
	v_cvt_pk_bf16_f32 v191, v100, v101
	global_store_dwordx2 v245, v[188:189], s[56:57]
	global_store_dwordx2 v245, v[190:191], s[56:57] offset:32
	v_cvt_pk_bf16_f32 v192, v38, v39
	v_cvt_pk_bf16_f32 v193, v40, v41
	v_cvt_pk_bf16_f32 v194, v34, v35
	v_cvt_pk_bf16_f32 v195, v36, v37
	global_store_dwordx2 v245, v[192:193], s[56:57] offset:256
	global_store_dwordx2 v245, v[194:195], s[56:57] offset:288
	v_add_u32_e32 v245, 0x120000, v187
	v_cvt_pk_bf16_f32 v188, v110, v111
	v_cvt_pk_bf16_f32 v189, v112, v113
	v_cvt_pk_bf16_f32 v190, v106, v107
	v_cvt_pk_bf16_f32 v191, v108, v109
	global_store_dwordx2 v245, v[188:189], s[56:57]
	global_store_dwordx2 v245, v[190:191], s[56:57] offset:32
	v_cvt_pk_bf16_f32 v192, v46, v47
	v_cvt_pk_bf16_f32 v193, v48, v49
	v_cvt_pk_bf16_f32 v194, v42, v43
	v_cvt_pk_bf16_f32 v195, v44, v45
	global_store_dwordx2 v245, v[192:193], s[56:57] offset:256
	global_store_dwordx2 v245, v[194:195], s[56:57] offset:288
	v_add_u32_e32 v245, 0x140000, v187
	v_cvt_pk_bf16_f32 v188, v118, v119
	v_cvt_pk_bf16_f32 v189, v120, v121
	v_cvt_pk_bf16_f32 v190, v114, v115
	v_cvt_pk_bf16_f32 v191, v116, v117
	global_store_dwordx2 v245, v[188:189], s[56:57]
	global_store_dwordx2 v245, v[190:191], s[56:57] offset:32
	v_cvt_pk_bf16_f32 v192, v54, v55
	v_cvt_pk_bf16_f32 v193, v56, v57
	v_cvt_pk_bf16_f32 v194, v50, v51
	v_cvt_pk_bf16_f32 v195, v52, v53
	global_store_dwordx2 v245, v[192:193], s[56:57] offset:256
	global_store_dwordx2 v245, v[194:195], s[56:57] offset:288
	v_add_u32_e32 v245, 0x160000, v187
	v_cvt_pk_bf16_f32 v188, v126, v127
	v_cvt_pk_bf16_f32 v189, v128, v129
	v_cvt_pk_bf16_f32 v190, v122, v123
	v_cvt_pk_bf16_f32 v191, v124, v125
	global_store_dwordx2 v245, v[188:189], s[56:57]
	global_store_dwordx2 v245, v[190:191], s[56:57] offset:32
	v_cvt_pk_bf16_f32 v192, v62, v63
	v_cvt_pk_bf16_f32 v193, v64, v65
	v_cvt_pk_bf16_f32 v194, v58, v59
	v_cvt_pk_bf16_f32 v195, v60, v61
	global_store_dwordx2 v245, v[192:193], s[56:57] offset:256
	global_store_dwordx2 v245, v[194:195], s[56:57] offset:288
	s_cmp_gt_u32 s89, 63
	s_cbranch_scc1 .LBB0_373
	s_memrealtime s[12:13]
	s_lshl_b32 s14, s10, 6
	s_ashr_i32 s15, s14, 31
	s_lshl_b64 s[14:15], s[14:15], 2
	s_add_u32 s14, s3, s14
	s_addc_u32 s15, s80, s15
	s_branch .LBB0_360

.LBB0_1054:
	s_lshl_b32 s60, s14, 8
	s_add_i32 s63, s63, s60
	v_lshrrev_b32_e32 v130, 2, v185
	v_or_b32_e32 v132, s63, v186
	v_and_b32_e32 v135, 12, v130
	s_lshl_b32 s61, s15, 5
	v_or_b32_e32 v130, s45, v135
	v_ashrrev_i32_e32 v133, 31, v132
	v_or_b32_e32 v140, s61, v130
	v_lshlrev_b64 v[130:131], 13, v[132:133]
	v_lshl_add_u64 v[130:131], s[56:57], 0, v[130:131]
	v_readlane_b32 s6, v246, 3
	v_lshlrev_b32_e32 v162, 1, v140
	v_lshlrev_b32_e32 v134, 2, v140
	v_readlane_b32 s7, v246, 4
	v_lshl_add_u64 v[130:131], v[130:131], 0, v[162:163]
	s_barrier
	v_lshl_add_u32 v244, v132, 13, v162
	s_nop 4
	global_load_dwordx4 v[220:223], v134, s[6:7]
	global_load_dwordx4 v[224:227], v134, s[6:7] offset:64
	global_load_dwordx4 v[228:231], v134, s[6:7] offset:512
	global_load_dwordx4 v[232:235], v134, s[6:7] offset:576
	global_load_dwordx2 v[188:189], v244, s[56:57]
	global_load_dwordx2 v[190:191], v244, s[56:57] offset:32
	global_load_dwordx2 v[192:193], v244, s[56:57] offset:256
	global_load_dwordx2 v[194:195], v244, s[56:57] offset:288
	v_add_u32_e32 v187, 0x20000, v244
	global_load_dwordx2 v[196:197], v187, s[56:57]
	global_load_dwordx2 v[198:199], v187, s[56:57] offset:32
	global_load_dwordx2 v[200:201], v187, s[56:57] offset:256
	global_load_dwordx2 v[202:203], v187, s[56:57] offset:288
	v_add_u32_e32 v187, 0x40000, v244
	global_load_dwordx2 v[204:205], v187, s[56:57]
	global_load_dwordx2 v[206:207], v187, s[56:57] offset:32
	global_load_dwordx2 v[208:209], v187, s[56:57] offset:256
	global_load_dwordx2 v[210:211], v187, s[56:57] offset:288
	v_add_u32_e32 v187, 0x60000, v244
	global_load_dwordx2 v[212:213], v187, s[56:57]
	global_load_dwordx2 v[214:215], v187, s[56:57] offset:32
	global_load_dwordx2 v[216:217], v187, s[56:57] offset:256
	global_load_dwordx2 v[218:219], v187, s[56:57] offset:288
	v_cvt_f32_i32_e32 v71, v71
	v_cvt_f32_i32_e32 v70, v70
	v_cvt_f32_i32_e32 v73, v73
	v_cvt_f32_i32_e32 v72, v72
	v_cvt_f32_i32_e32 v35, v35
	v_cvt_f32_i32_e32 v34, v34
	v_cvt_f32_i32_e32 v37, v37
	v_cvt_f32_i32_e32 v36, v36
	v_cvt_f32_i32_e32 v19, v19
	v_cvt_f32_i32_e32 v18, v18
	v_cvt_f32_i32_e32 v21, v21
	v_cvt_f32_i32_e32 v20, v20
	v_cvt_f32_i32_e32 v3, v3
	v_cvt_f32_i32_e32 v2, v2
	v_cvt_f32_i32_e32 v5, v5
	v_cvt_f32_i32_e32 v4, v4
	v_cvt_f32_i32_e32 v103, v103
	v_cvt_f32_i32_e32 v102, v102
	v_cvt_f32_i32_e32 v105, v105
	v_cvt_f32_i32_e32 v104, v104
	v_cvt_f32_i32_e32 v55, v55
	v_cvt_f32_i32_e32 v54, v54
	v_cvt_f32_i32_e32 v57, v57
	v_cvt_f32_i32_e32 v56, v56
	v_cvt_f32_i32_e32 v39, v39
	v_cvt_f32_i32_e32 v38, v38
	v_cvt_f32_i32_e32 v41, v41
	v_cvt_f32_i32_e32 v40, v40
	v_cvt_f32_i32_e32 v7, v7
	v_cvt_f32_i32_e32 v6, v6
	v_cvt_f32_i32_e32 v9, v9
	v_cvt_f32_i32_e32 v8, v8
	v_cvt_f32_i32_e32 v115, v115
	v_cvt_f32_i32_e32 v114, v114
	v_cvt_f32_i32_e32 v117, v117
	v_cvt_f32_i32_e32 v116, v116
	v_cvt_f32_i32_e32 v87, v87
	v_cvt_f32_i32_e32 v86, v86
	v_cvt_f32_i32_e32 v89, v89
	v_cvt_f32_i32_e32 v88, v88
	v_cvt_f32_i32_e32 v67, v67
	v_cvt_f32_i32_e32 v66, v66
	v_cvt_f32_i32_e32 v69, v69
	v_cvt_f32_i32_e32 v68, v68
	v_cvt_f32_i32_e32 v27, v27
	v_cvt_f32_i32_e32 v26, v26
	v_cvt_f32_i32_e32 v29, v29
	v_cvt_f32_i32_e32 v28, v28
	v_cvt_f32_i32_e32 v127, v127
	v_cvt_f32_i32_e32 v126, v126
	v_cvt_f32_i32_e32 v129, v129
	v_cvt_f32_i32_e32 v128, v128
	v_cvt_f32_i32_e32 v111, v111
	v_cvt_f32_i32_e32 v110, v110
	v_cvt_f32_i32_e32 v113, v113
	v_cvt_f32_i32_e32 v112, v112
	v_cvt_f32_i32_e32 v91, v91
	v_cvt_f32_i32_e32 v90, v90
	v_cvt_f32_i32_e32 v93, v93
	v_cvt_f32_i32_e32 v92, v92
	v_cvt_f32_i32_e32 v51, v51
	v_cvt_f32_i32_e32 v50, v50
	v_cvt_f32_i32_e32 v53, v53
	v_cvt_f32_i32_e32 v52, v52
	v_cvt_f32_i32_e32 v123, v123
	v_cvt_f32_i32_e32 v122, v122
	v_cvt_f32_i32_e32 v125, v125
	v_cvt_f32_i32_e32 v124, v124
	v_cvt_f32_i32_e32 v119, v119
	v_cvt_f32_i32_e32 v118, v118
	v_cvt_f32_i32_e32 v121, v121
	v_cvt_f32_i32_e32 v120, v120
	v_cvt_f32_i32_e32 v107, v107
	v_cvt_f32_i32_e32 v106, v106
	v_cvt_f32_i32_e32 v109, v109
	v_cvt_f32_i32_e32 v108, v108
	v_cvt_f32_i32_e32 v83, v83
	v_cvt_f32_i32_e32 v82, v82
	v_cvt_f32_i32_e32 v85, v85
	v_cvt_f32_i32_e32 v84, v84
	v_cvt_f32_i32_e32 v99, v99
	v_cvt_f32_i32_e32 v98, v98
	v_cvt_f32_i32_e32 v101, v101
	v_cvt_f32_i32_e32 v100, v100
	v_cvt_f32_i32_e32 v95, v95
	v_cvt_f32_i32_e32 v94, v94
	v_cvt_f32_i32_e32 v97, v97
	v_cvt_f32_i32_e32 v96, v96
	v_cvt_f32_i32_e32 v79, v79
	v_cvt_f32_i32_e32 v78, v78
	v_cvt_f32_i32_e32 v81, v81
	v_cvt_f32_i32_e32 v80, v80
	v_cvt_f32_i32_e32 v75, v75
	v_cvt_f32_i32_e32 v74, v74
	v_cvt_f32_i32_e32 v77, v77
	v_cvt_f32_i32_e32 v76, v76
	v_cvt_f32_i32_e32 v63, v63
	v_cvt_f32_i32_e32 v62, v62
	v_cvt_f32_i32_e32 v65, v65
	v_cvt_f32_i32_e32 v64, v64
	v_cvt_f32_i32_e32 v59, v59
	v_cvt_f32_i32_e32 v58, v58
	v_cvt_f32_i32_e32 v61, v61
	v_cvt_f32_i32_e32 v60, v60
	v_cvt_f32_i32_e32 v47, v47
	v_cvt_f32_i32_e32 v46, v46
	v_cvt_f32_i32_e32 v49, v49
	v_cvt_f32_i32_e32 v48, v48
	v_cvt_f32_i32_e32 v43, v43
	v_cvt_f32_i32_e32 v42, v42
	v_cvt_f32_i32_e32 v45, v45
	v_cvt_f32_i32_e32 v44, v44
	v_cvt_f32_i32_e32 v31, v31
	v_cvt_f32_i32_e32 v30, v30
	v_cvt_f32_i32_e32 v33, v33
	v_cvt_f32_i32_e32 v32, v32
	v_cvt_f32_i32_e32 v23, v23
	v_cvt_f32_i32_e32 v22, v22
	v_cvt_f32_i32_e32 v25, v25
	v_cvt_f32_i32_e32 v24, v24
	v_cvt_f32_i32_e32 v15, v15
	v_cvt_f32_i32_e32 v14, v14
	v_cvt_f32_i32_e32 v17, v17
	v_cvt_f32_i32_e32 v16, v16
	v_cvt_f32_i32_e32 v11, v11
	v_cvt_f32_i32_e32 v10, v10
	v_cvt_f32_i32_e32 v13, v13
	v_cvt_f32_i32_e32 v12, v12
	s_waitcnt vmcnt(16)
	v_pk_mul_f32 v[220:221], v[220:221], s[38:39] op_sel_hi:[1,0]
	v_pk_mul_f32 v[222:223], v[222:223], s[38:39] op_sel_hi:[1,0]
	v_pk_mul_f32 v[224:225], v[224:225], s[38:39] op_sel_hi:[1,0]
	v_pk_mul_f32 v[226:227], v[226:227], s[38:39] op_sel_hi:[1,0]
	v_pk_mul_f32 v[228:229], v[228:229], s[38:39] op_sel_hi:[1,0]
	v_pk_mul_f32 v[230:231], v[230:231], s[38:39] op_sel_hi:[1,0]
	v_pk_mul_f32 v[232:233], v[232:233], s[38:39] op_sel_hi:[1,0]
	v_pk_mul_f32 v[234:235], v[234:235], s[38:39] op_sel_hi:[1,0]
	s_waitcnt vmcnt(14)
	v_lshlrev_b32_e32 v236, 16, v188
	v_and_b32_e32 v237, 0xffff0000, v188
	v_lshlrev_b32_e32 v238, 16, v189
	v_and_b32_e32 v239, 0xffff0000, v189
	v_lshlrev_b32_e32 v240, 16, v190
	v_and_b32_e32 v241, 0xffff0000, v190
	v_lshlrev_b32_e32 v242, 16, v191
	v_and_b32_e32 v243, 0xffff0000, v191
	v_pk_fma_f32 v[72:73], v[222:223], v[72:73], v[238:239]
	v_pk_fma_f32 v[70:71], v[220:221], v[70:71], v[236:237]
	v_pk_fma_f32 v[36:37], v[226:227], v[36:37], v[242:243]
	v_pk_fma_f32 v[34:35], v[224:225], v[34:35], v[240:241]
	v_add_u32_e32 v187, 0x100000, v244
	global_load_dwordx2 v[188:189], v187, s[56:57]
	global_load_dwordx2 v[190:191], v187, s[56:57] offset:32
	s_waitcnt vmcnt(14)
	v_lshlrev_b32_e32 v236, 16, v192
	v_and_b32_e32 v237, 0xffff0000, v192
	v_lshlrev_b32_e32 v238, 16, v193
	v_and_b32_e32 v239, 0xffff0000, v193
	v_lshlrev_b32_e32 v240, 16, v194
	v_and_b32_e32 v241, 0xffff0000, v194
	v_lshlrev_b32_e32 v242, 16, v195
	v_and_b32_e32 v243, 0xffff0000, v195
	v_pk_fma_f32 v[20:21], v[230:231], v[20:21], v[238:239]
	v_pk_fma_f32 v[18:19], v[228:229], v[18:19], v[236:237]
	v_pk_fma_f32 v[4:5], v[234:235], v[4:5], v[242:243]
	v_pk_fma_f32 v[2:3], v[232:233], v[2:3], v[240:241]
	global_load_dwordx2 v[192:193], v187, s[56:57] offset:256
	global_load_dwordx2 v[194:195], v187, s[56:57] offset:288
	s_waitcnt vmcnt(14)
	v_lshlrev_b32_e32 v236, 16, v196
	v_and_b32_e32 v237, 0xffff0000, v196
	v_lshlrev_b32_e32 v238, 16, v197
	v_and_b32_e32 v239, 0xffff0000, v197
	v_lshlrev_b32_e32 v240, 16, v198
	v_and_b32_e32 v241, 0xffff0000, v198
	v_lshlrev_b32_e32 v242, 16, v199
	v_and_b32_e32 v243, 0xffff0000, v199
	v_pk_fma_f32 v[104:105], v[222:223], v[104:105], v[238:239]
	v_pk_fma_f32 v[102:103], v[220:221], v[102:103], v[236:237]
	v_pk_fma_f32 v[56:57], v[226:227], v[56:57], v[242:243]
	v_pk_fma_f32 v[54:55], v[224:225], v[54:55], v[240:241]
	v_add_u32_e32 v187, 0x120000, v244
	global_load_dwordx2 v[196:197], v187, s[56:57]
	global_load_dwordx2 v[198:199], v187, s[56:57] offset:32
	s_waitcnt vmcnt(14)
	v_lshlrev_b32_e32 v236, 16, v200
	v_and_b32_e32 v237, 0xffff0000, v200
	v_lshlrev_b32_e32 v238, 16, v201
	v_and_b32_e32 v239, 0xffff0000, v201
	v_lshlrev_b32_e32 v240, 16, v202
	v_and_b32_e32 v241, 0xffff0000, v202
	v_lshlrev_b32_e32 v242, 16, v203
	v_and_b32_e32 v243, 0xffff0000, v203
	v_pk_fma_f32 v[40:41], v[230:231], v[40:41], v[238:239]
	v_pk_fma_f32 v[38:39], v[228:229], v[38:39], v[236:237]
	v_pk_fma_f32 v[8:9], v[234:235], v[8:9], v[242:243]
	v_pk_fma_f32 v[6:7], v[232:233], v[6:7], v[240:241]
	global_load_dwordx2 v[200:201], v187, s[56:57] offset:256
	global_load_dwordx2 v[202:203], v187, s[56:57] offset:288
	s_waitcnt vmcnt(14)
	v_lshlrev_b32_e32 v236, 16, v204
	v_and_b32_e32 v237, 0xffff0000, v204
	v_lshlrev_b32_e32 v238, 16, v205
	v_and_b32_e32 v239, 0xffff0000, v205
	v_lshlrev_b32_e32 v240, 16, v206
	v_and_b32_e32 v241, 0xffff0000, v206
	v_lshlrev_b32_e32 v242, 16, v207
	v_and_b32_e32 v243, 0xffff0000, v207
	v_pk_fma_f32 v[116:117], v[222:223], v[116:117], v[238:239]
	v_pk_fma_f32 v[114:115], v[220:221], v[114:115], v[236:237]
	v_pk_fma_f32 v[88:89], v[226:227], v[88:89], v[242:243]
	v_pk_fma_f32 v[86:87], v[224:225], v[86:87], v[240:241]
	v_add_u32_e32 v187, 0x140000, v244
	global_load_dwordx2 v[204:205], v187, s[56:57]
	global_load_dwordx2 v[206:207], v187, s[56:57] offset:32
	s_waitcnt vmcnt(14)
	v_lshlrev_b32_e32 v236, 16, v208
	v_and_b32_e32 v237, 0xffff0000, v208
	v_lshlrev_b32_e32 v238, 16, v209
	v_and_b32_e32 v239, 0xffff0000, v209
	v_lshlrev_b32_e32 v240, 16, v210
	v_and_b32_e32 v241, 0xffff0000, v210
	v_lshlrev_b32_e32 v242, 16, v211
	v_and_b32_e32 v243, 0xffff0000, v211
	v_pk_fma_f32 v[68:69], v[230:231], v[68:69], v[238:239]
	v_pk_fma_f32 v[66:67], v[228:229], v[66:67], v[236:237]
	v_pk_fma_f32 v[28:29], v[234:235], v[28:29], v[242:243]
	v_pk_fma_f32 v[26:27], v[232:233], v[26:27], v[240:241]
	global_load_dwordx2 v[208:209], v187, s[56:57] offset:256
	global_load_dwordx2 v[210:211], v187, s[56:57] offset:288
	s_waitcnt vmcnt(14)
	v_lshlrev_b32_e32 v236, 16, v212
	v_and_b32_e32 v237, 0xffff0000, v212
	v_lshlrev_b32_e32 v238, 16, v213
	v_and_b32_e32 v239, 0xffff0000, v213
	v_lshlrev_b32_e32 v240, 16, v214
	v_and_b32_e32 v241, 0xffff0000, v214
	v_lshlrev_b32_e32 v242, 16, v215
	v_and_b32_e32 v243, 0xffff0000, v215
	v_pk_fma_f32 v[128:129], v[222:223], v[128:129], v[238:239]
	v_pk_fma_f32 v[126:127], v[220:221], v[126:127], v[236:237]
	v_pk_fma_f32 v[112:113], v[226:227], v[112:113], v[242:243]
	v_pk_fma_f32 v[110:111], v[224:225], v[110:111], v[240:241]
	v_add_u32_e32 v187, 0x160000, v244
	global_load_dwordx2 v[212:213], v187, s[56:57]
	global_load_dwordx2 v[214:215], v187, s[56:57] offset:32
	s_waitcnt vmcnt(14)
	v_lshlrev_b32_e32 v236, 16, v216
	v_and_b32_e32 v237, 0xffff0000, v216
	v_lshlrev_b32_e32 v238, 16, v217
	v_and_b32_e32 v239, 0xffff0000, v217
	v_lshlrev_b32_e32 v240, 16, v218
	v_and_b32_e32 v241, 0xffff0000, v218
	v_lshlrev_b32_e32 v242, 16, v219
	v_and_b32_e32 v243, 0xffff0000, v219
	v_pk_fma_f32 v[92:93], v[230:231], v[92:93], v[238:239]
	v_pk_fma_f32 v[90:91], v[228:229], v[90:91], v[236:237]
	v_pk_fma_f32 v[52:53], v[234:235], v[52:53], v[242:243]
	v_pk_fma_f32 v[50:51], v[232:233], v[50:51], v[240:241]
	global_load_dwordx2 v[216:217], v187, s[56:57] offset:256
	global_load_dwordx2 v[218:219], v187, s[56:57] offset:288
	s_waitcnt vmcnt(14)
	v_lshlrev_b32_e32 v236, 16, v188
	v_and_b32_e32 v237, 0xffff0000, v188
	v_lshlrev_b32_e32 v238, 16, v189
	v_and_b32_e32 v239, 0xffff0000, v189
	v_lshlrev_b32_e32 v240, 16, v190
	v_and_b32_e32 v241, 0xffff0000, v190
	v_lshlrev_b32_e32 v242, 16, v191
	v_and_b32_e32 v243, 0xffff0000, v191
	v_pk_fma_f32 v[124:125], v[222:223], v[124:125], v[238:239]
	v_pk_fma_f32 v[122:123], v[220:221], v[122:123], v[236:237]
	v_pk_fma_f32 v[120:121], v[226:227], v[120:121], v[242:243]
	v_pk_fma_f32 v[118:119], v[224:225], v[118:119], v[240:241]
	s_waitcnt vmcnt(12)
	v_lshlrev_b32_e32 v236, 16, v192
	v_and_b32_e32 v237, 0xffff0000, v192
	v_lshlrev_b32_e32 v238, 16, v193
	v_and_b32_e32 v239, 0xffff0000, v193
	v_lshlrev_b32_e32 v240, 16, v194
	v_and_b32_e32 v241, 0xffff0000, v194
	v_lshlrev_b32_e32 v242, 16, v195
	v_and_b32_e32 v243, 0xffff0000, v195
	v_pk_fma_f32 v[108:109], v[230:231], v[108:109], v[238:239]
	v_pk_fma_f32 v[106:107], v[228:229], v[106:107], v[236:237]
	v_pk_fma_f32 v[84:85], v[234:235], v[84:85], v[242:243]
	v_pk_fma_f32 v[82:83], v[232:233], v[82:83], v[240:241]
	s_waitcnt vmcnt(10)
	v_lshlrev_b32_e32 v236, 16, v196
	v_and_b32_e32 v237, 0xffff0000, v196
	v_lshlrev_b32_e32 v238, 16, v197
	v_and_b32_e32 v239, 0xffff0000, v197
	v_lshlrev_b32_e32 v240, 16, v198
	v_and_b32_e32 v241, 0xffff0000, v198
	v_lshlrev_b32_e32 v242, 16, v199
	v_and_b32_e32 v243, 0xffff0000, v199
	v_pk_fma_f32 v[100:101], v[222:223], v[100:101], v[238:239]
	v_pk_fma_f32 v[98:99], v[220:221], v[98:99], v[236:237]
	v_pk_fma_f32 v[96:97], v[226:227], v[96:97], v[242:243]
	v_pk_fma_f32 v[94:95], v[224:225], v[94:95], v[240:241]
	s_waitcnt vmcnt(8)
	v_lshlrev_b32_e32 v236, 16, v200
	v_and_b32_e32 v237, 0xffff0000, v200
	v_lshlrev_b32_e32 v238, 16, v201
	v_and_b32_e32 v239, 0xffff0000, v201
	v_lshlrev_b32_e32 v240, 16, v202
	v_and_b32_e32 v241, 0xffff0000, v202
	v_lshlrev_b32_e32 v242, 16, v203
	v_and_b32_e32 v243, 0xffff0000, v203
	v_pk_fma_f32 v[80:81], v[230:231], v[80:81], v[238:239]
	v_pk_fma_f32 v[78:79], v[228:229], v[78:79], v[236:237]
	v_pk_fma_f32 v[76:77], v[234:235], v[76:77], v[242:243]
	v_pk_fma_f32 v[74:75], v[232:233], v[74:75], v[240:241]
	s_waitcnt vmcnt(6)
	v_lshlrev_b32_e32 v236, 16, v204
	v_and_b32_e32 v237, 0xffff0000, v204
	v_lshlrev_b32_e32 v238, 16, v205
	v_and_b32_e32 v239, 0xffff0000, v205
	v_lshlrev_b32_e32 v240, 16, v206
	v_and_b32_e32 v241, 0xffff0000, v206
	v_lshlrev_b32_e32 v242, 16, v207
	v_and_b32_e32 v243, 0xffff0000, v207
	v_pk_fma_f32 v[64:65], v[222:223], v[64:65], v[238:239]
	v_pk_fma_f32 v[62:63], v[220:221], v[62:63], v[236:237]
	v_pk_fma_f32 v[60:61], v[226:227], v[60:61], v[242:243]
	v_pk_fma_f32 v[58:59], v[224:225], v[58:59], v[240:241]
	s_waitcnt vmcnt(4)
	v_lshlrev_b32_e32 v236, 16, v208
	v_and_b32_e32 v237, 0xffff0000, v208
	v_lshlrev_b32_e32 v238, 16, v209
	v_and_b32_e32 v239, 0xffff0000, v209
	v_lshlrev_b32_e32 v240, 16, v210
	v_and_b32_e32 v241, 0xffff0000, v210
	v_lshlrev_b32_e32 v242, 16, v211
	v_and_b32_e32 v243, 0xffff0000, v211
	v_pk_fma_f32 v[48:49], v[230:231], v[48:49], v[238:239]
	v_pk_fma_f32 v[46:47], v[228:229], v[46:47], v[236:237]
	v_pk_fma_f32 v[44:45], v[234:235], v[44:45], v[242:243]
	v_pk_fma_f32 v[42:43], v[232:233], v[42:43], v[240:241]
	s_waitcnt vmcnt(2)
	v_lshlrev_b32_e32 v236, 16, v212
	v_and_b32_e32 v237, 0xffff0000, v212
	v_lshlrev_b32_e32 v238, 16, v213
	v_and_b32_e32 v239, 0xffff0000, v213
	v_lshlrev_b32_e32 v240, 16, v214
	v_and_b32_e32 v241, 0xffff0000, v214
	v_lshlrev_b32_e32 v242, 16, v215
	v_and_b32_e32 v243, 0xffff0000, v215
	v_pk_fma_f32 v[32:33], v[222:223], v[32:33], v[238:239]
	v_pk_fma_f32 v[30:31], v[220:221], v[30:31], v[236:237]
	v_pk_fma_f32 v[24:25], v[226:227], v[24:25], v[242:243]
	v_pk_fma_f32 v[22:23], v[224:225], v[22:23], v[240:241]
	s_waitcnt vmcnt(0)
	v_lshlrev_b32_e32 v236, 16, v216
	v_and_b32_e32 v237, 0xffff0000, v216
	v_lshlrev_b32_e32 v238, 16, v217
	v_and_b32_e32 v239, 0xffff0000, v217
	v_lshlrev_b32_e32 v240, 16, v218
	v_and_b32_e32 v241, 0xffff0000, v218
	v_lshlrev_b32_e32 v242, 16, v219
	v_and_b32_e32 v243, 0xffff0000, v219
	v_pk_fma_f32 v[16:17], v[230:231], v[16:17], v[238:239]
	v_pk_fma_f32 v[14:15], v[228:229], v[14:15], v[236:237]
	v_pk_fma_f32 v[12:13], v[234:235], v[12:13], v[242:243]
	v_pk_fma_f32 v[10:11], v[232:233], v[10:11], v[240:241]
	s_lshl_b32 s4, s15, 2
	v_mul_f32_e32 v152, v37, v37
	v_fmac_f32_e32 v152, v36, v36
	v_mul_f32_e32 v153, v5, v5
	v_fmac_f32_e32 v153, v4, v4
	v_mul_f32_e32 v138, v73, v73
	v_mul_f32_e32 v136, v71, v71
	v_mul_f32_e32 v139, v35, v35
	v_fmac_f32_e32 v136, v70, v70
	v_fmac_f32_e32 v138, v72, v72
	v_fmac_f32_e32 v139, v34, v34
	v_add_f32_e32 v136, v136, v138
	v_add_f32_e32 v138, v139, v152
	v_and_b32_e32 v133, 64, v1
	v_add_f32_e32 v136, v136, v138
	v_mul_f32_e32 v138, v19, v19
	v_mul_f32_e32 v139, v21, v21
	v_xor_b32_e32 v132, 16, v1
	v_add_u32_e32 v133, 64, v133
	v_mul_f32_e32 v152, v3, v3
	v_fmac_f32_e32 v138, v18, v18
	v_fmac_f32_e32 v139, v20, v20
	v_cmp_lt_i32_e32 vcc, v132, v133
	v_fmac_f32_e32 v152, v2, v2
	v_add_f32_e32 v138, v138, v139
	v_cndmask_b32_e32 v132, v1, v132, vcc
	v_add_f32_e32 v139, v152, v153
	v_add_f32_e32 v136, v136, v138
	v_lshlrev_b32_e32 v132, 2, v132
	v_add_f32_e32 v136, v139, v136
	ds_bpermute_b32 v138, v132, v136
	v_xor_b32_e32 v139, 32, v1
	v_cmp_lt_i32_e32 vcc, v139, v133
	v_and_b32_e32 v137, 63, v185
	s_add_i32 s6, s4, 0
	v_cndmask_b32_e32 v133, v1, v139, vcc
	v_lshlrev_b32_e32 v133, 2, v133
	s_waitcnt lgkmcnt(0)
	v_add_f32_e32 v136, v136, v138
	ds_bpermute_b32 v138, v133, v136
	v_cmp_gt_u32_e32 vcc, 16, v137
	s_and_saveexec_b64 s[4:5], vcc
	s_cbranch_execz .LBB0_1056
	s_lshl_b32 s7, s19, 10
	s_add_i32 s7, s6, s7
	v_lshl_add_u32 v130, v186, 4, s7
	s_waitcnt lgkmcnt(0)
	v_add_f32_e32 v131, v136, v138
	ds_write_b32 v130, v131

.LBB0_1439:
	s_lshl_b32 s67, s42, 8
	s_add_i32 s4, s66, s67
	v_lshrrev_b32_e32 v2, 2, v189
	v_or_b32_e32 v10, s4, v188
	v_and_b32_e32 v160, 12, v2
	s_lshl_b32 s68, s8, 5
	v_or_b32_e32 v2, s59, v160
	v_ashrrev_i32_e32 v11, 31, v10
	v_or_b32_e32 v161, s68, v2
	v_lshlrev_b64 v[2:3], 13, v[10:11]
	v_lshl_add_u64 v[2:3], s[56:57], 0, v[2:3]
	v_lshlrev_b32_e32 v154, 1, v161
	v_lshl_add_u64 v[158:159], v[2:3], 0, v[154:155]
	s_barrier
	v_lshl_add_u32 v232, v10, 13, v154
	global_load_dwordx2 v[192:193], v232, s[56:57]
	global_load_dwordx2 v[194:195], v232, s[56:57] offset:32
	global_load_dwordx2 v[196:197], v232, s[56:57] offset:256
	global_load_dwordx2 v[198:199], v232, s[56:57] offset:288
	v_add_u32_e32 v234, 0x20000, v232
	global_load_dwordx2 v[200:201], v234, s[56:57]
	global_load_dwordx2 v[202:203], v234, s[56:57] offset:32
	global_load_dwordx2 v[204:205], v234, s[56:57] offset:256
	global_load_dwordx2 v[206:207], v234, s[56:57] offset:288
	v_add_u32_e32 v234, 0x40000, v232
	global_load_dwordx2 v[208:209], v234, s[56:57]
	global_load_dwordx2 v[210:211], v234, s[56:57] offset:32
	global_load_dwordx2 v[212:213], v234, s[56:57] offset:256
	global_load_dwordx2 v[214:215], v234, s[56:57] offset:288
	v_add_u32_e32 v234, 0x60000, v232
	global_load_dwordx2 v[216:217], v234, s[56:57]
	global_load_dwordx2 v[218:219], v234, s[56:57] offset:32
	global_load_dwordx2 v[220:221], v234, s[56:57] offset:256
	global_load_dwordx2 v[222:223], v234, s[56:57] offset:288
	s_waitcnt vmcnt(14)
	v_lshlrev_b32_e32 v224, 16, v192
	v_and_b32_e32 v225, 0xffff0000, v192
	v_lshlrev_b32_e32 v226, 16, v193
	v_and_b32_e32 v227, 0xffff0000, v193
	v_lshlrev_b32_e32 v228, 16, v194
	v_and_b32_e32 v229, 0xffff0000, v194
	v_lshlrev_b32_e32 v230, 16, v195
	v_and_b32_e32 v231, 0xffff0000, v195
	v_pk_fma_f32 v[72:73], v[32:33], s[40:41], v[226:227] op_sel_hi:[1,0,1]
	v_pk_fma_f32 v[70:71], v[30:31], s[40:41], v[224:225] op_sel_hi:[1,0,1]
	v_pk_fma_f32 v[32:33], v[152:153], s[40:41], v[230:231] op_sel_hi:[1,0,1]
	v_pk_fma_f32 v[30:31], v[150:151], s[40:41], v[228:229] op_sel_hi:[1,0,1]
	v_add_u32_e32 v234, 0x100000, v232
	global_load_dwordx2 v[192:193], v234, s[56:57]
	global_load_dwordx2 v[194:195], v234, s[56:57] offset:32
	s_waitcnt vmcnt(14)
	v_lshlrev_b32_e32 v224, 16, v196
	v_and_b32_e32 v225, 0xffff0000, v196
	v_lshlrev_b32_e32 v226, 16, v197
	v_and_b32_e32 v227, 0xffff0000, v197
	v_lshlrev_b32_e32 v228, 16, v198
	v_and_b32_e32 v229, 0xffff0000, v198
	v_lshlrev_b32_e32 v230, 16, v199
	v_and_b32_e32 v231, 0xffff0000, v199
	v_pk_fma_f32 v[16:17], v[144:145], s[40:41], v[226:227] op_sel_hi:[1,0,1]
	v_pk_fma_f32 v[14:15], v[142:143], s[40:41], v[224:225] op_sel_hi:[1,0,1]
	v_pk_fma_f32 v[4:5], v[148:149], s[40:41], v[230:231] op_sel_hi:[1,0,1]
	v_pk_fma_f32 v[2:3], v[146:147], s[40:41], v[228:229] op_sel_hi:[1,0,1]
	global_load_dwordx2 v[196:197], v234, s[56:57] offset:256
	global_load_dwordx2 v[198:199], v234, s[56:57] offset:288
	s_waitcnt vmcnt(14)
	v_lshlrev_b32_e32 v224, 16, v200
	v_and_b32_e32 v225, 0xffff0000, v200
	v_lshlrev_b32_e32 v226, 16, v201
	v_and_b32_e32 v227, 0xffff0000, v201
	v_lshlrev_b32_e32 v228, 16, v202
	v_and_b32_e32 v229, 0xffff0000, v202
	v_lshlrev_b32_e32 v230, 16, v203
	v_and_b32_e32 v231, 0xffff0000, v203
	v_pk_fma_f32 v[92:93], v[92:93], s[40:41], v[226:227] op_sel_hi:[1,0,1]
	v_pk_fma_f32 v[90:91], v[90:91], s[40:41], v[224:225] op_sel_hi:[1,0,1]
	v_pk_fma_f32 v[44:45], v[44:45], s[40:41], v[230:231] op_sel_hi:[1,0,1]
	v_pk_fma_f32 v[42:43], v[42:43], s[40:41], v[228:229] op_sel_hi:[1,0,1]
	v_add_u32_e32 v234, 0x120000, v232
	global_load_dwordx2 v[200:201], v234, s[56:57]
	global_load_dwordx2 v[202:203], v234, s[56:57] offset:32
	s_waitcnt vmcnt(14)
	v_lshlrev_b32_e32 v224, 16, v204
	v_and_b32_e32 v225, 0xffff0000, v204
	v_lshlrev_b32_e32 v226, 16, v205
	v_and_b32_e32 v227, 0xffff0000, v205
	v_lshlrev_b32_e32 v228, 16, v206
	v_and_b32_e32 v229, 0xffff0000, v206
	v_lshlrev_b32_e32 v230, 16, v207
	v_and_b32_e32 v231, 0xffff0000, v207
	v_pk_fma_f32 v[28:29], v[28:29], s[40:41], v[226:227] op_sel_hi:[1,0,1]
	v_pk_fma_f32 v[26:27], v[26:27], s[40:41], v[224:225] op_sel_hi:[1,0,1]
	v_pk_fma_f32 v[8:9], v[140:141], s[40:41], v[230:231] op_sel_hi:[1,0,1]
	v_pk_fma_f32 v[6:7], v[138:139], s[40:41], v[228:229] op_sel_hi:[1,0,1]
	global_load_dwordx2 v[204:205], v234, s[56:57] offset:256
	global_load_dwordx2 v[206:207], v234, s[56:57] offset:288
	s_waitcnt vmcnt(14)
	v_lshlrev_b32_e32 v224, 16, v208
	v_and_b32_e32 v225, 0xffff0000, v208
	v_lshlrev_b32_e32 v226, 16, v209
	v_and_b32_e32 v227, 0xffff0000, v209
	v_lshlrev_b32_e32 v228, 16, v210
	v_and_b32_e32 v229, 0xffff0000, v210
	v_lshlrev_b32_e32 v230, 16, v211
	v_and_b32_e32 v231, 0xffff0000, v211
	v_pk_fma_f32 v[116:117], v[116:117], s[40:41], v[226:227] op_sel_hi:[1,0,1]
	v_pk_fma_f32 v[114:115], v[114:115], s[40:41], v[224:225] op_sel_hi:[1,0,1]
	v_pk_fma_f32 v[64:65], v[64:65], s[40:41], v[230:231] op_sel_hi:[1,0,1]
	v_pk_fma_f32 v[62:63], v[62:63], s[40:41], v[228:229] op_sel_hi:[1,0,1]
	v_add_u32_e32 v234, 0x140000, v232
	global_load_dwordx2 v[208:209], v234, s[56:57]
	global_load_dwordx2 v[210:211], v234, s[56:57] offset:32
	s_waitcnt vmcnt(14)
	v_lshlrev_b32_e32 v224, 16, v212
	v_and_b32_e32 v225, 0xffff0000, v212
	v_lshlrev_b32_e32 v226, 16, v213
	v_and_b32_e32 v227, 0xffff0000, v213
	v_lshlrev_b32_e32 v228, 16, v214
	v_and_b32_e32 v229, 0xffff0000, v214
	v_lshlrev_b32_e32 v230, 16, v215
	v_and_b32_e32 v231, 0xffff0000, v215
	v_pk_fma_f32 v[40:41], v[40:41], s[40:41], v[226:227] op_sel_hi:[1,0,1]
	v_pk_fma_f32 v[38:39], v[38:39], s[40:41], v[224:225] op_sel_hi:[1,0,1]
	v_pk_fma_f32 v[12:13], v[128:129], s[40:41], v[230:231] op_sel_hi:[1,0,1]
	v_pk_fma_f32 v[10:11], v[126:127], s[40:41], v[228:229] op_sel_hi:[1,0,1]
	global_load_dwordx2 v[212:213], v234, s[56:57] offset:256
	global_load_dwordx2 v[214:215], v234, s[56:57] offset:288
	s_waitcnt vmcnt(14)
	v_lshlrev_b32_e32 v224, 16, v216
	v_and_b32_e32 v225, 0xffff0000, v216
	v_lshlrev_b32_e32 v226, 16, v217
	v_and_b32_e32 v227, 0xffff0000, v217
	v_lshlrev_b32_e32 v228, 16, v218
	v_and_b32_e32 v229, 0xffff0000, v218
	v_lshlrev_b32_e32 v230, 16, v219
	v_and_b32_e32 v231, 0xffff0000, v219
	v_pk_fma_f32 v[128:129], v[80:81], s[40:41], v[226:227] op_sel_hi:[1,0,1]
	v_pk_fma_f32 v[126:127], v[78:79], s[40:41], v[224:225] op_sel_hi:[1,0,1]
	v_pk_fma_f32 v[80:81], v[52:53], s[40:41], v[230:231] op_sel_hi:[1,0,1]
	v_pk_fma_f32 v[78:79], v[50:51], s[40:41], v[228:229] op_sel_hi:[1,0,1]
	v_add_u32_e32 v234, 0x160000, v232
	global_load_dwordx2 v[216:217], v234, s[56:57]
	global_load_dwordx2 v[218:219], v234, s[56:57] offset:32
	s_waitcnt vmcnt(14)
	v_lshlrev_b32_e32 v224, 16, v220
	v_and_b32_e32 v225, 0xffff0000, v220
	v_lshlrev_b32_e32 v226, 16, v221
	v_and_b32_e32 v227, 0xffff0000, v221
	v_lshlrev_b32_e32 v228, 16, v222
	v_and_b32_e32 v229, 0xffff0000, v222
	v_lshlrev_b32_e32 v230, 16, v223
	v_and_b32_e32 v231, 0xffff0000, v223
	v_pk_fma_f32 v[52:53], v[24:25], s[40:41], v[226:227] op_sel_hi:[1,0,1]
	v_pk_fma_f32 v[50:51], v[22:23], s[40:41], v[224:225] op_sel_hi:[1,0,1]
	v_pk_fma_f32 v[24:25], v[76:77], s[40:41], v[230:231] op_sel_hi:[1,0,1]
	v_pk_fma_f32 v[22:23], v[74:75], s[40:41], v[228:229] op_sel_hi:[1,0,1]
	global_load_dwordx2 v[220:221], v234, s[56:57] offset:256
	global_load_dwordx2 v[222:223], v234, s[56:57] offset:288
	s_waitcnt vmcnt(14)
	v_lshlrev_b32_e32 v224, 16, v192
	v_and_b32_e32 v225, 0xffff0000, v192
	v_lshlrev_b32_e32 v226, 16, v193
	v_and_b32_e32 v227, 0xffff0000, v193
	v_lshlrev_b32_e32 v228, 16, v194
	v_and_b32_e32 v229, 0xffff0000, v194
	v_lshlrev_b32_e32 v230, 16, v195
	v_and_b32_e32 v231, 0xffff0000, v195
	v_pk_fma_f32 v[136:137], v[136:137], s[40:41], v[226:227] op_sel_hi:[1,0,1]
	v_pk_fma_f32 v[134:135], v[134:135], s[40:41], v[224:225] op_sel_hi:[1,0,1]
	v_pk_fma_f32 v[104:105], v[104:105], s[40:41], v[230:231] op_sel_hi:[1,0,1]
	v_pk_fma_f32 v[102:103], v[102:103], s[40:41], v[228:229] op_sel_hi:[1,0,1]
	s_waitcnt vmcnt(12)
	v_lshlrev_b32_e32 v224, 16, v196
	v_and_b32_e32 v225, 0xffff0000, v196
	v_lshlrev_b32_e32 v226, 16, v197
	v_and_b32_e32 v227, 0xffff0000, v197
	v_lshlrev_b32_e32 v228, 16, v198
	v_and_b32_e32 v229, 0xffff0000, v198
	v_lshlrev_b32_e32 v230, 16, v199
	v_and_b32_e32 v231, 0xffff0000, v199
	v_pk_fma_f32 v[76:77], v[36:37], s[40:41], v[226:227] op_sel_hi:[1,0,1]
	v_pk_fma_f32 v[74:75], v[34:35], s[40:41], v[224:225] op_sel_hi:[1,0,1]
	v_pk_fma_f32 v[36:37], v[132:133], s[40:41], v[230:231] op_sel_hi:[1,0,1]
	v_pk_fma_f32 v[34:35], v[130:131], s[40:41], v[228:229] op_sel_hi:[1,0,1]
	s_waitcnt vmcnt(10)
	v_lshlrev_b32_e32 v224, 16, v200
	v_and_b32_e32 v225, 0xffff0000, v200
	v_lshlrev_b32_e32 v226, 16, v201
	v_and_b32_e32 v227, 0xffff0000, v201
	v_lshlrev_b32_e32 v228, 16, v202
	v_and_b32_e32 v229, 0xffff0000, v202
	v_lshlrev_b32_e32 v230, 16, v203
	v_and_b32_e32 v231, 0xffff0000, v203
	v_pk_fma_f32 v[132:133], v[124:125], s[40:41], v[226:227] op_sel_hi:[1,0,1]
	v_pk_fma_f32 v[130:131], v[122:123], s[40:41], v[224:225] op_sel_hi:[1,0,1]
	v_pk_fma_f32 v[124:125], v[100:101], s[40:41], v[230:231] op_sel_hi:[1,0,1]
	v_pk_fma_f32 v[122:123], v[98:99], s[40:41], v[228:229] op_sel_hi:[1,0,1]
	s_waitcnt vmcnt(8)
	v_lshlrev_b32_e32 v224, 16, v204
	v_and_b32_e32 v225, 0xffff0000, v204
	v_lshlrev_b32_e32 v226, 16, v205
	v_and_b32_e32 v227, 0xffff0000, v205
	v_lshlrev_b32_e32 v228, 16, v206
	v_and_b32_e32 v229, 0xffff0000, v206
	v_lshlrev_b32_e32 v230, 16, v207
	v_and_b32_e32 v231, 0xffff0000, v207
	v_pk_fma_f32 v[100:101], v[48:49], s[40:41], v[226:227] op_sel_hi:[1,0,1]
	v_pk_fma_f32 v[98:99], v[46:47], s[40:41], v[224:225] op_sel_hi:[1,0,1]
	v_pk_fma_f32 v[48:49], v[120:121], s[40:41], v[230:231] op_sel_hi:[1,0,1]
	v_pk_fma_f32 v[46:47], v[118:119], s[40:41], v[228:229] op_sel_hi:[1,0,1]
	s_waitcnt vmcnt(6)
	v_lshlrev_b32_e32 v224, 16, v208
	v_and_b32_e32 v225, 0xffff0000, v208
	v_lshlrev_b32_e32 v226, 16, v209
	v_and_b32_e32 v227, 0xffff0000, v209
	v_lshlrev_b32_e32 v228, 16, v210
	v_and_b32_e32 v229, 0xffff0000, v210
	v_lshlrev_b32_e32 v230, 16, v211
	v_and_b32_e32 v231, 0xffff0000, v211
	v_pk_fma_f32 v[120:121], v[112:113], s[40:41], v[226:227] op_sel_hi:[1,0,1]
	v_pk_fma_f32 v[118:119], v[110:111], s[40:41], v[224:225] op_sel_hi:[1,0,1]
	v_pk_fma_f32 v[112:113], v[108:109], s[40:41], v[230:231] op_sel_hi:[1,0,1]
	v_pk_fma_f32 v[110:111], v[106:107], s[40:41], v[228:229] op_sel_hi:[1,0,1]
	s_waitcnt vmcnt(4)
	v_lshlrev_b32_e32 v224, 16, v212
	v_and_b32_e32 v225, 0xffff0000, v212
	v_lshlrev_b32_e32 v226, 16, v213
	v_and_b32_e32 v227, 0xffff0000, v213
	v_lshlrev_b32_e32 v228, 16, v214
	v_and_b32_e32 v229, 0xffff0000, v214
	v_lshlrev_b32_e32 v230, 16, v215
	v_and_b32_e32 v231, 0xffff0000, v215
	v_pk_fma_f32 v[108:109], v[68:69], s[40:41], v[226:227] op_sel_hi:[1,0,1]
	v_pk_fma_f32 v[106:107], v[66:67], s[40:41], v[224:225] op_sel_hi:[1,0,1]
	v_pk_fma_f32 v[68:69], v[96:97], s[40:41], v[230:231] op_sel_hi:[1,0,1]
	v_pk_fma_f32 v[66:67], v[94:95], s[40:41], v[228:229] op_sel_hi:[1,0,1]
	s_waitcnt vmcnt(2)
	v_lshlrev_b32_e32 v224, 16, v216
	v_and_b32_e32 v225, 0xffff0000, v216
	v_lshlrev_b32_e32 v226, 16, v217
	v_and_b32_e32 v227, 0xffff0000, v217
	v_lshlrev_b32_e32 v228, 16, v218
	v_and_b32_e32 v229, 0xffff0000, v218
	v_lshlrev_b32_e32 v230, 16, v219
	v_and_b32_e32 v231, 0xffff0000, v219
	v_pk_fma_f32 v[96:97], v[88:89], s[40:41], v[226:227] op_sel_hi:[1,0,1]
	v_pk_fma_f32 v[94:95], v[86:87], s[40:41], v[224:225] op_sel_hi:[1,0,1]
	v_pk_fma_f32 v[88:89], v[84:85], s[40:41], v[230:231] op_sel_hi:[1,0,1]
	v_pk_fma_f32 v[86:87], v[82:83], s[40:41], v[228:229] op_sel_hi:[1,0,1]
	s_waitcnt vmcnt(0)
	v_lshlrev_b32_e32 v224, 16, v220
	v_and_b32_e32 v225, 0xffff0000, v220
	v_lshlrev_b32_e32 v226, 16, v221
	v_and_b32_e32 v227, 0xffff0000, v221
	v_lshlrev_b32_e32 v228, 16, v222
	v_and_b32_e32 v229, 0xffff0000, v222
	v_lshlrev_b32_e32 v230, 16, v223
	v_and_b32_e32 v231, 0xffff0000, v223
	v_pk_fma_f32 v[84:85], v[56:57], s[40:41], v[226:227] op_sel_hi:[1,0,1]
	v_pk_fma_f32 v[82:83], v[54:55], s[40:41], v[224:225] op_sel_hi:[1,0,1]
	v_pk_fma_f32 v[56:57], v[60:61], s[40:41], v[230:231] op_sel_hi:[1,0,1]
	v_pk_fma_f32 v[54:55], v[58:59], s[40:41], v[228:229] op_sel_hi:[1,0,1]
	s_lshl_b32 s4, s8, 2
	s_add_i32 s8, s4, 0
	v_mul_f32_e32 v141, v71, v71
	v_mul_f32_e32 v142, v73, v73
	v_mul_f32_e32 v143, v31, v31
	v_mul_f32_e32 v146, v33, v33
	v_fmac_f32_e32 v141, v70, v70
	v_fmac_f32_e32 v142, v72, v72
	v_fmac_f32_e32 v143, v30, v30
	v_fmac_f32_e32 v146, v32, v32
	v_add_f32_e32 v141, v141, v142
	v_add_f32_e32 v142, v143, v146
	v_and_b32_e32 v140, 64, v1
	v_add_f32_e32 v141, v141, v142
	v_mul_f32_e32 v142, v15, v15
	v_mul_f32_e32 v143, v17, v17
	v_xor_b32_e32 v138, 16, v1
	v_add_u32_e32 v140, 64, v140
	v_mul_f32_e32 v146, v3, v3
	v_mul_f32_e32 v147, v5, v5
	v_fmac_f32_e32 v142, v14, v14
	v_fmac_f32_e32 v143, v16, v16
	v_cmp_lt_i32_e32 vcc, v138, v140
	v_fmac_f32_e32 v146, v2, v2
	v_fmac_f32_e32 v147, v4, v4
	v_add_f32_e32 v142, v142, v143
	v_cndmask_b32_e32 v138, v1, v138, vcc
	v_add_f32_e32 v143, v146, v147
	v_add_f32_e32 v141, v141, v142
	v_lshlrev_b32_e32 v138, 2, v138
	v_add_f32_e32 v141, v143, v141
	ds_bpermute_b32 v142, v138, v141
	v_xor_b32_e32 v143, 32, v1
	v_cmp_lt_i32_e32 vcc, v143, v140
	v_and_b32_e32 v139, 63, v189
	s_waitcnt lgkmcnt(0)
	v_add_f32_e32 v141, v141, v142
	v_cndmask_b32_e32 v140, v1, v143, vcc
	v_lshlrev_b32_e32 v140, 2, v140
	ds_bpermute_b32 v142, v140, v141
	v_cmp_gt_u32_e32 vcc, 16, v139
	s_and_saveexec_b64 s[4:5], vcc
	s_cbranch_execz .LBB0_1441
	s_lshl_b32 s9, s7, 10
	s_add_i32 s9, s8, s9
	v_lshl_add_u32 v58, v188, 4, s9
	s_waitcnt lgkmcnt(0)
	v_add_f32_e32 v59, v141, v142
	ds_write_b32 v58, v59

.LBB0_1460:
	s_or_b64 exec, exec, s[18:19]
	v_cvt_pk_bf16_f32 v224, v70, v71
	v_cvt_pk_bf16_f32 v225, v72, v73
	v_cvt_pk_bf16_f32 v226, v30, v31
	v_cvt_pk_bf16_f32 v227, v32, v33
	global_store_dwordx2 v232, v[224:225], s[56:57]
	global_store_dwordx2 v232, v[226:227], s[56:57] offset:32
	v_cvt_pk_bf16_f32 v228, v14, v15
	v_cvt_pk_bf16_f32 v229, v16, v17
	v_cvt_pk_bf16_f32 v230, v2, v3
	v_cvt_pk_bf16_f32 v231, v4, v5
	global_store_dwordx2 v232, v[228:229], s[56:57] offset:256
	global_store_dwordx2 v232, v[230:231], s[56:57] offset:288
	v_add_u32_e32 v233, 0x20000, v232
	v_cvt_pk_bf16_f32 v224, v90, v91
	v_cvt_pk_bf16_f32 v225, v92, v93
	v_cvt_pk_bf16_f32 v226, v42, v43
	v_cvt_pk_bf16_f32 v227, v44, v45
	global_store_dwordx2 v233, v[224:225], s[56:57]
	global_store_dwordx2 v233, v[226:227], s[56:57] offset:32
	v_cvt_pk_bf16_f32 v228, v26, v27
	v_cvt_pk_bf16_f32 v229, v28, v29
	v_cvt_pk_bf16_f32 v230, v6, v7
	v_cvt_pk_bf16_f32 v231, v8, v9
	global_store_dwordx2 v233, v[228:229], s[56:57] offset:256
	global_store_dwordx2 v233, v[230:231], s[56:57] offset:288
	v_add_u32_e32 v233, 0x40000, v232
	v_cvt_pk_bf16_f32 v224, v114, v115
	v_cvt_pk_bf16_f32 v225, v116, v117
	v_cvt_pk_bf16_f32 v226, v62, v63
	v_cvt_pk_bf16_f32 v227, v64, v65
	global_store_dwordx2 v233, v[224:225], s[56:57]
	global_store_dwordx2 v233, v[226:227], s[56:57] offset:32
	v_cvt_pk_bf16_f32 v228, v38, v39
	v_cvt_pk_bf16_f32 v229, v40, v41
	v_cvt_pk_bf16_f32 v230, v10, v11
	v_cvt_pk_bf16_f32 v231, v12, v13
	global_store_dwordx2 v233, v[228:229], s[56:57] offset:256
	global_store_dwordx2 v233, v[230:231], s[56:57] offset:288
	v_add_u32_e32 v233, 0x60000, v232
	v_cvt_pk_bf16_f32 v224, v126, v127
	v_cvt_pk_bf16_f32 v225, v128, v129
	v_cvt_pk_bf16_f32 v226, v78, v79
	v_cvt_pk_bf16_f32 v227, v80, v81
	global_store_dwordx2 v233, v[224:225], s[56:57]
	global_store_dwordx2 v233, v[226:227], s[56:57] offset:32
	v_cvt_pk_bf16_f32 v228, v50, v51
	v_cvt_pk_bf16_f32 v229, v52, v53
	v_cvt_pk_bf16_f32 v230, v22, v23
	v_cvt_pk_bf16_f32 v231, v24, v25
	global_store_dwordx2 v233, v[228:229], s[56:57] offset:256
	global_store_dwordx2 v233, v[230:231], s[56:57] offset:288
	v_add_u32_e32 v233, 0x100000, v232
	v_cvt_pk_bf16_f32 v224, v134, v135
	v_cvt_pk_bf16_f32 v225, v136, v137
	v_cvt_pk_bf16_f32 v226, v102, v103
	v_cvt_pk_bf16_f32 v227, v104, v105
	global_store_dwordx2 v233, v[224:225], s[56:57]
	global_store_dwordx2 v233, v[226:227], s[56:57] offset:32
	v_cvt_pk_bf16_f32 v228, v74, v75
	v_cvt_pk_bf16_f32 v229, v76, v77
	v_cvt_pk_bf16_f32 v230, v34, v35
	v_cvt_pk_bf16_f32 v231, v36, v37
	global_store_dwordx2 v233, v[228:229], s[56:57] offset:256
	global_store_dwordx2 v233, v[230:231], s[56:57] offset:288
	v_add_u32_e32 v233, 0x120000, v232
	v_cvt_pk_bf16_f32 v224, v130, v131
	v_cvt_pk_bf16_f32 v225, v132, v133
	v_cvt_pk_bf16_f32 v226, v122, v123
	v_cvt_pk_bf16_f32 v227, v124, v125
	global_store_dwordx2 v233, v[224:225], s[56:57]
	global_store_dwordx2 v233, v[226:227], s[56:57] offset:32
	v_cvt_pk_bf16_f32 v228, v98, v99
	v_cvt_pk_bf16_f32 v229, v100, v101
	v_cvt_pk_bf16_f32 v230, v46, v47
	v_cvt_pk_bf16_f32 v231, v48, v49
	global_store_dwordx2 v233, v[228:229], s[56:57] offset:256
	global_store_dwordx2 v233, v[230:231], s[56:57] offset:288
	v_add_u32_e32 v233, 0x140000, v232
	v_cvt_pk_bf16_f32 v224, v118, v119
	v_cvt_pk_bf16_f32 v225, v120, v121
	v_cvt_pk_bf16_f32 v226, v110, v111
	v_cvt_pk_bf16_f32 v227, v112, v113
	global_store_dwordx2 v233, v[224:225], s[56:57]
	global_store_dwordx2 v233, v[226:227], s[56:57] offset:32
	v_cvt_pk_bf16_f32 v228, v106, v107
	v_cvt_pk_bf16_f32 v229, v108, v109
	v_cvt_pk_bf16_f32 v230, v66, v67
	v_cvt_pk_bf16_f32 v231, v68, v69
	global_store_dwordx2 v233, v[228:229], s[56:57] offset:256
	global_store_dwordx2 v233, v[230:231], s[56:57] offset:288
	v_add_u32_e32 v233, 0x160000, v232
	v_cvt_pk_bf16_f32 v224, v94, v95
	v_cvt_pk_bf16_f32 v225, v96, v97
	v_cvt_pk_bf16_f32 v226, v86, v87
	v_cvt_pk_bf16_f32 v227, v88, v89
	global_store_dwordx2 v233, v[224:225], s[56:57]
	global_store_dwordx2 v233, v[226:227], s[56:57] offset:32
	v_cvt_pk_bf16_f32 v228, v82, v83
	v_cvt_pk_bf16_f32 v229, v84, v85
	v_cvt_pk_bf16_f32 v230, v54, v55
	v_cvt_pk_bf16_f32 v231, v56, v57
	global_store_dwordx2 v233, v[228:229], s[56:57] offset:256
	global_store_dwordx2 v233, v[230:231], s[56:57] offset:288
	s_cmp_gt_u32 s65, 63
	s_cbranch_scc1 .LBB0_1477
	s_memrealtime s[18:19]
	s_lshl_b32 s42, s42, 6
	s_ashr_i32 s43, s42, 31
	s_lshl_b64 s[42:43], s[42:43], 2
	s_add_u32 s42, s41, s42
	s_addc_u32 s43, s50, s43
	s_branch .LBB0_1464
